# even-layer mixer M1/M3 loop-top waits changed to counted waits so the previous iteration's stores stay in flight
# speedup vs baseline: 1.0116x; 1.0116x over previous
.LBB0_320:
	s_add_u32 s12, s0, 0x11fff000
	s_addc_u32 s13, s1, 0
	v_and_b32_e32 v87, 63, v24
	s_add_u32 s14, s0, 0x240ff000
	s_waitcnt vmcnt(5)
	v_cvt_pk_bf16_f32 v5, v5, v8
	v_add_u32_e32 v8, s4, v87
	s_movk_i32 s21, 0x1a00
	v_mov_b64_e32 v[32:33], s[12:13]
	v_add_u32_e32 v34, 0x200, v24
	s_addc_u32 s15, s1, 0
	v_cvt_pk_bf16_f32 v4, v4, v6
	s_waitcnt vmcnt(3)
	v_cvt_pk_bf16_f32 v6, v9, v10
	v_mad_i64_i32 v[8:9], s[2:3], v8, s21, v[32:33]
	s_mov_b32 s17, 0
	s_lshl_b32 s16, s31, 8
	v_ashrrev_i32_e32 v31, 3, v34
	v_lshl_add_u64 v[8:9], v[8:9], 0, s[16:17]
	s_mov_b64 s[18:19], 0x1400
	v_and_b32_e32 v16, -8, v31
	v_ashrrev_i32_e32 v88, 3, v24
	v_lshl_add_u64 v[8:9], v[8:9], 0, s[18:19]
	v_ashrrev_i32_e32 v17, 31, v16
	v_and_b32_e32 v18, -8, v88
	v_add_u32_e32 v23, s4, v86
	v_lshl_add_u64 v[36:37], v[16:17], 1, v[8:9]
	v_ashrrev_i32_e32 v19, 31, v18
	v_add_u32_e32 v21, 48, v23
	v_lshl_add_u64 v[38:39], v[18:19], 1, v[8:9]
	global_load_dwordx4 v[12:15], v[36:37], off
	global_load_dwordx4 v[8:11], v[38:39], off
	v_mad_i64_i32 v[36:37], s[2:3], v21, s21, v[32:33]
	v_readlane_b32 s2, v242, 20
	s_lshl_b32 s16, s2, 1
	v_lshl_add_u64 v[36:37], v[36:37], 0, s[16:17]
	v_lshlrev_b32_e32 v20, 1, v20
	v_mov_b32_e32 v21, 0
	v_and_b32_e32 v28, 12, v28
	v_add_u32_e32 v35, 32, v23
	v_lshl_add_u64 v[36:37], v[36:37], 0, v[20:21]
	v_lshlrev_b32_e32 v28, 1, v28
	v_mov_b32_e32 v29, v21
	v_mad_i64_i32 v[38:39], s[2:3], v35, s21, v[32:33]
	v_lshl_add_u64 v[36:37], v[36:37], 0, v[28:29]
	s_movk_i32 s5, 0x1000
	v_lshl_add_u64 v[38:39], v[38:39], 0, s[16:17]
	v_add_u32_e32 v35, 16, v23
	v_add_co_u32_e32 v36, vcc, s5, v36
	v_lshl_add_u64 v[38:39], v[38:39], 0, v[20:21]
	v_mad_i64_i32 v[40:41], s[2:3], v35, s21, v[32:33]
	v_addc_co_u32_e32 v37, vcc, 0, v37, vcc
	v_lshl_add_u64 v[38:39], v[38:39], 0, v[28:29]
	v_lshl_add_u64 v[40:41], v[40:41], 0, s[16:17]
	v_add_co_u32_e32 v38, vcc, s5, v38
	v_lshl_add_u64 v[40:41], v[40:41], 0, v[20:21]
	v_mad_i64_i32 v[42:43], s[2:3], v23, s21, v[32:33]
	v_addc_co_u32_e32 v39, vcc, 0, v39, vcc
	v_lshl_add_u64 v[40:41], v[40:41], 0, v[28:29]
	v_lshl_add_u64 v[42:43], v[42:43], 0, s[16:17]
	v_add_co_u32_e32 v40, vcc, s5, v40
	v_lshl_add_u64 v[42:43], v[42:43], 0, v[20:21]
	s_nop 0
	v_addc_co_u32_e32 v41, vcc, 0, v41, vcc
	v_lshl_add_u64 v[42:43], v[42:43], 0, v[28:29]
	v_add_u32_e32 v23, s4, v88
	v_add_co_u32_e32 v50, vcc, s5, v42
	v_mad_i64_i32 v[32:33], s[2:3], v23, s21, v[32:33]
	v_lshlrev_b32_e32 v23, 2, v24
	v_addc_co_u32_e32 v51, vcc, 0, v43, vcc
	global_load_dwordx2 v[42:43], v[36:37], off offset:512
	global_load_dwordx2 v[44:45], v[38:39], off offset:512
	global_load_dwordx2 v[46:47], v[40:41], off offset:512
	global_load_dwordx2 v[48:49], v[50:51], off offset:512
	v_and_b32_e32 v36, 28, v23
	v_lshlrev_b32_e32 v38, 1, v36
	v_mov_b32_e32 v39, v21
	v_lshl_add_u64 v[32:33], v[32:33], 0, v[38:39]
	v_add_co_u32_e32 v32, vcc, s5, v32
	s_waitcnt vmcnt(7)
	v_cvt_pk_bf16_f32 v26, v26, v27
	v_addc_co_u32_e32 v33, vcc, 0, v33, vcc
	global_load_dwordx2 v[32:33], v[32:33], off offset:2048
	s_movk_i32 s2, 0x50
	v_and_b32_e32 v4, v7, v4
	v_and_b32_e32 v5, v7, v5
	v_and_b32_e32 v6, v7, v6
	v_and_b32_e32 v7, v7, v26
	v_mul_lo_u32 v26, v88, s2
	s_movk_i32 s9, 0x90
	v_add3_u32 v89, 0, v26, v38
	v_mul_lo_u32 v26, v18, s9
	v_lshlrev_b32_e32 v27, 1, v87
	v_add3_u32 v90, 0, v26, v27
	v_mul_lo_u32 v26, v16, s9
	v_add3_u32 v91, 0, v26, v27
	v_and_b32_e32 v26, 48, v24
	s_movk_i32 s2, 0xff
	v_and_b32_e32 v92, 0xc0, v23
	v_ashrrev_i32_e32 v23, 2, v24
	v_lshl_add_u32 v37, v86, 1, 0
	v_add_u32_e32 v39, 0, v26
	v_cmp_lt_u32_e64 s[4:5], s2, v24
	v_and_b32_e32 v26, -16, v23
	s_movk_i32 s2, 0x2400
	v_mad_i32_i24 v50, v22, s2, v37
	v_lshl_or_b32 v94, v22, 5, s31
	v_or_b32_e32 v22, v26, v86
	v_lshl_add_u32 v38, v25, 4, 0
	s_lshl_b32 s8, s31, 7
	v_and_b32_e32 v41, 48, v23
	v_mad_u64_u32 v[22:23], s[2:3], v22, s9, v[38:39]
	s_add_u32 s2, s12, s16
	v_or_b32_e32 v27, v30, v41
	v_ashrrev_i32_e32 v35, 31, v34
	s_addc_u32 s3, s13, 0
	v_or_b32_e32 v23, v30, v26
	v_lshlrev_b32_e32 v25, 4, v24
	v_mul_u32_u24_e32 v53, 0x90, v27
	v_lshlrev_b64 v[26:27], 3, v[34:35]
	v_lshl_add_u64 v[34:35], s[2:3], 0, v[20:21]
	v_lshlrev_b32_e32 v20, 2, v41
	v_and_b32_e32 v25, 0x70, v25
	v_lshl_add_u64 v[28:29], v[34:35], 0, v[28:29]
	v_lshl_add_u64 v[34:35], s[0:1], 0, v[20:21]
	v_lshlrev_b32_e32 v20, 2, v30
	v_mul_u32_u24_e32 v40, 0x50, v86
	v_add_u32_e32 v51, 0, v25
	v_mul_lo_u32 v52, v88, s9
	v_mul_u32_u24_e32 v54, 0x90, v86
	v_mul_lo_u32 v55, v23, s9
	v_ashrrev_i32_e32 v25, 31, v24
	v_mul_lo_u32 v56, v31, s9
	v_lshl_add_u64 v[30:31], v[34:35], 0, v[20:21]
	s_mov_b64 s[0:1], 0x32af000
	v_or_b32_e32 v93, 60, v92
	v_cmp_ne_u32_e64 s[6:7], 0, v86
	v_lshlrev_b64 v[24:25], 3, v[24:25]
	v_lshl_add_u64 v[30:31], v[30:31], 0, s[0:1]
	s_movk_i32 s24, 0x44
	v_lshlrev_b32_e32 v20, 1, v36
	s_lshl_b32 s16, s8, 1
	v_add_u32_e32 v23, v39, v40
	s_mov_b32 s25, 0xbfb8aa3b
	s_mov_b32 s26, 0x800000
	s_mov_b32 s27, 0x3f317217
	s_mov_b32 s28, 0x7f800000
	s_mov_b32 s20, 0x3d800000
	v_add_u32_e32 v95, v50, v53
	v_add_u32_e32 v96, v38, v54
	v_add_u32_e32 v97, v37, v55
	v_add_u32_e32 v98, v51, v52
	s_mov_b32 s29, 0xc3e00000
	v_add_u32_e32 v99, v51, v56
	v_mov_b32_e32 v100, 0x41b17218
	v_mov_b32_e32 v101, 0x44
	v_mov_b32_e32 v102, 0x43e00000
	v_readlane_b32 s2, v242, 0
	s_waitcnt vmcnt(4)
	v_mov_b64_e32 v[40:41], v[42:43]
	s_waitcnt vmcnt(3)
	v_mov_b64_e32 v[38:39], v[44:45]
	s_waitcnt vmcnt(1)
	v_mov_b64_e32 v[34:35], v[48:49]
	v_mov_b64_e32 v[36:37], v[46:47]
	s_waitcnt vmcnt(0)
	s_branch .LBB0_322

.LBB0_322:
	v_readlane_b32 s0, v242, 11
	s_add_i32 s30, s2, s0
	s_cmpk_gt_i32 s30, 0x87f
	s_cselect_b64 s[22:23], -1, 0
	s_and_b64 vcc, exec, s[22:23]
	s_waitcnt vmcnt(4)
	ds_write_b64 v89, v[32:33] offset:36864
	ds_write_b16 v90, v8
	ds_write_b16_d16_hi v90, v8 offset:144
	ds_write_b16 v90, v9 offset:288
	ds_write_b16_d16_hi v90, v9 offset:432
	ds_write_b16 v90, v10 offset:576
	ds_write_b16_d16_hi v90, v10 offset:720
	ds_write_b16 v90, v11 offset:864
	ds_write_b16_d16_hi v90, v11 offset:1008
	ds_write_b16 v91, v12
	ds_write_b16_d16_hi v91, v12 offset:144
	ds_write_b16 v91, v13 offset:288
	ds_write_b16_d16_hi v91, v13 offset:432
	ds_write_b16 v91, v14 offset:576
	ds_write_b16_d16_hi v91, v14 offset:720
	ds_write_b16 v91, v15 offset:864
	ds_write_b16_d16_hi v91, v15 offset:1008
	s_waitcnt lgkmcnt(0)
	s_barrier
	v_readlane_b32 s1, v242, 12
	s_cbranch_vccnz .LBB0_328
	s_ashr_i32 s0, s30, 2
	s_mul_hi_i32 s1, s0, 0x78787879
	s_lshr_b32 s3, s1, 31
	s_ashr_i32 s8, s1, 5
	s_add_i32 s8, s8, s3
	s_mul_i32 s1, s8, 0x44
	s_sub_i32 s0, s0, s1
	s_lshl_b32 s9, s0, 6
	s_cmp_gt_i32 s0, 3
	s_mov_b64 s[0:1], -1
	s_cbranch_scc0 .LBB0_325
	s_lshl_b32 s0, s8, 12
	s_add_i32 s0, s9, s0
	s_add_i32 s3, s0, 0xffffff00
	s_mov_b64 s[0:1], 0

.LBB0_388:
	s_or_b64 exec, exec, s[0:1]
	s_waitcnt lgkmcnt(0)
	v_mov_b32_e32 v0, v208
	v_readlane_b32 s0, v242, 6
	s_barrier
	s_nop 0
	s_mov_b32 s2, 0
	s_nop 0
	v_add_u32_e32 v44, s0, v0
	s_mov_b32 s0, 0x20000
	v_cmp_gt_i32_e32 vcc, s0, v44
	s_and_saveexec_b64 s[0:1], vcc
	s_cbranch_execz .LBB0_397
	v_readlane_b32 s4, v242, 1
	v_readlane_b32 s5, v242, 2
	s_load_dwordx2 s[4:5], s[4:5], s2 offset:0x108
	v_mov_b32_e32 v33, 0
	s_mov_b64 s[2:3], 0
	s_mov_b32 s16, 0x1ffff
	s_mov_b32 s18, 0xc3e00000
	s_waitcnt lgkmcnt(0)
	s_add_u32 s6, s4, 0x32af000
	s_addc_u32 s7, s5, 0
	s_add_u32 s8, s4, 0x240ff000
	s_addc_u32 s9, s5, 0
	s_add_u32 s12, s4, 0x284ff000
	s_addc_u32 s13, s5, 0
	v_readlane_b32 s4, v242, 11
	s_lshl_b32 s17, s4, 9
	v_mov_b32_e32 v45, 5
	v_mov_b32_e32 v46, 0x43e00000
	v_mov_b32_e32 v47, 0
	v_mov_b32_e32 v48, 0
	v_mov_b32_e32 v49, 0
	v_mov_b32_e32 v50, 0
	v_readlane_b32 s5, v242, 12

.LBB0_456:
	s_add_u32 s4, s0, 0x1fcff000
	s_addc_u32 s5, s1, 0
	v_readlane_b32 s0, v242, 25
	v_readlane_b32 s1, v242, 26
	v_lshlrev_b32_e32 v33, 2, v8
	s_and_b64 vcc, exec, s[0:1]
	s_cbranch_vccnz .LBB0_489
	s_waitcnt vmcnt(11)
	v_cvt_pk_bf16_f32 v8, v9, v44
	s_waitcnt vmcnt(9)
	v_cvt_pk_bf16_f32 v9, v10, v45
	s_waitcnt vmcnt(7)
	v_cvt_pk_bf16_f32 v10, v46, v48
	v_lshlrev_b32_e32 v48, 2, v40
	v_ashrrev_i32_e32 v117, 3, v40
	s_movk_i32 s0, 0x50
	v_and_b32_e32 v70, 28, v48
	v_mul_lo_u32 v41, v117, s0
	s_add_i32 s0, 0, 0x1c200
	v_lshlrev_b32_e32 v44, 1, v70
	v_add_u32_e32 v54, 0x200, v40
	v_add3_u32 v118, s0, v41, v44
	v_and_b32_e32 v119, 63, v40
	v_and_b32_e32 v44, -8, v117
	s_movk_i32 s1, 0x90
	v_ashrrev_i32_e32 v62, 3, v54
	v_mul_lo_u32 v41, v44, s1
	v_lshlrev_b32_e32 v45, 1, v119
	v_and_b32_e32 v46, -8, v62
	v_add3_u32 v120, 0, v41, v45
	v_mul_lo_u32 v41, v46, s1
	v_add3_u32 v121, 0, v41, v45
	v_lshlrev_b32_e32 v41, 4, v40
	v_and_b32_e32 v41, 0x70, v41
	s_waitcnt vmcnt(5)
	v_cvt_pk_bf16_f32 v35, v47, v49
	v_add_u32_e32 v122, 0, v41
	v_ashrrev_i32_e32 v41, 31, v40
	v_and_b32_e32 v8, v11, v8
	v_and_b32_e32 v9, v11, v9
	v_and_b32_e32 v10, v11, v10
	v_and_b32_e32 v11, v11, v35
	v_bfe_u32 v35, v40, 6, 2
	v_lshlrev_b64 v[50:51], 3, v[40:41]
	v_and_b32_e32 v41, 48, v40
	v_lshlrev_b32_e32 v63, 4, v35
	v_add_u32_e32 v71, s0, v41
	s_movk_i32 s0, 0xff
	v_and_b32_e32 v41, 0xc0, v48
	v_mul_i32_i24_e32 v48, 0x1200, v34
	v_or_b32_e32 v124, v33, v63
	v_cmp_lt_u32_e64 s[6:7], s0, v40
	v_or3_b32 v33, v63, v48, v33
	s_movk_i32 s0, 0x48
	v_lshlrev_b32_e32 v48, 1, v34
	v_or_b32_e32 v63, v63, v112
	v_add_u32_e32 v72, 0, v32
	v_mad_u32_u24 v33, v112, s0, v33
	v_mad_u32_u24 v126, v63, s1, v72
	v_mul_u32_u24_e32 v63, 0x48, v63
	v_and_b32_e32 v64, 0xffffff00, v40
	s_add_i32 s3, 0, 0x1c000
	v_lshlrev_b32_e32 v65, 6, v35
	v_readlane_b32 s33, v242, 24
	v_lshl_add_u32 v130, v33, 1, 0
	v_or_b32_e32 v33, 1, v48
	s_add_i32 s2, 0, 0x16800
	v_lshlrev_b32_e32 v63, 1, v63
	v_add3_u32 v74, s3, v64, v65
	v_or_b32_e32 v64, s33, v112
	v_mul_lo_u32 v129, v62, s1
	v_lshl_or_b32 v62, v33, 4, v112
	v_lshl_or_b32 v34, v34, 5, v112
	v_mul_u32_u24_e32 v73, 0x50, v112
	v_add3_u32 v127, s2, v63, v32
	v_or_b32_e32 v63, v36, v112
	v_add_u32_e32 v68, v64, v36
	v_cmp_le_i32_e64 s[14:15], v48, v35
	v_lshlrev_b32_e32 v64, 1, v34
	v_or_b32_e32 v131, 1, v124
	v_or_b32_e32 v132, 2, v124
	v_or_b32_e32 v133, 3, v124
	v_cmp_lt_i32_e64 s[24:25], v48, v35
	v_cmp_ge_i32_e64 s[26:27], v48, v35
	v_lshlrev_b32_e32 v48, 1, v62
	s_add_i32 s0, 0, 0x18c00
	v_mul_lo_u32 v128, v117, s1
	v_cmp_gt_i32_e64 s[10:11], v62, v124
	v_cmp_lt_i32_e64 s[12:13], v62, v124
	v_mul_lo_u32 v75, v34, s1
	v_mul_lo_u32 v78, v62, s1
	v_cmp_gt_i32_e64 s[28:29], v62, v131
	v_cmp_gt_i32_e64 s[30:31], v62, v132
	v_cmp_gt_i32_e64 s[34:35], v62, v133
	v_add_u32_e32 v80, s0, v64
	v_cmp_ge_i32_e64 s[42:43], v33, v35
	v_add_u32_e32 v33, s0, v48
	v_cmp_lt_i32_e64 s[44:45], v62, v132
	v_cmp_lt_i32_e64 s[46:47], v62, v133
	v_mad_u64_u32 v[62:63], s[0:1], v63, s1, v[72:73]
	v_readlane_b32 s0, v242, 20
	s_lshl_b32 s0, s0, 1
	s_add_u32 s0, s50, s0
	v_mov_b32_e32 v49, 0
	v_and_b32_e32 v39, 12, v39
	v_add_u32_e32 v79, s2, v48
	s_addc_u32 s1, s51, 0
	v_lshlrev_b32_e32 v48, 1, v38
	s_lshl_b32 s56, s33, 1
	v_cmp_gt_i32_e64 s[16:17], v34, v124
	v_cmp_gt_i32_e64 s[18:19], v34, v131
	v_cmp_gt_i32_e64 s[20:21], v34, v132
	v_cmp_gt_i32_e64 s[22:23], v34, v133
	v_cmp_lt_i32_e64 s[36:37], v34, v124
	v_cmp_lt_i32_e64 s[38:39], v34, v132
	v_cmp_lt_i32_e64 s[40:41], v34, v133
	v_lshl_add_u64 v[34:35], s[0:1], 0, v[48:49]
	v_lshlrev_b32_e32 v48, 1, v39
	s_add_u32 s0, s50, s56
	v_add_u32_e32 v76, s2, v64
	v_lshl_add_u64 v[64:65], v[34:35], 0, v[48:49]
	s_addc_u32 s1, s51, 0
	v_lshlrev_b32_e32 v48, 1, v112
	v_ashrrev_i32_e32 v55, 31, v54
	v_mul_u32_u24_e32 v77, 0x90, v124
	v_ashrrev_i32_e32 v69, 31, v68
	v_lshl_add_u64 v[34:35], s[0:1], 0, v[48:49]
	s_mov_b32 s57, 0
	v_add_u32_e32 v123, 0xd800, v122
	v_ashrrev_i32_e32 v45, 31, v44
	v_ashrrev_i32_e32 v47, 31, v46
	v_lshlrev_b64 v[54:55], 3, v[54:55]
	v_or_b32_e32 v125, 60, v41
	v_cmp_eq_u32_e64 s[8:9], 0, v112
	v_add_u32_e32 v63, 0xd800, v62
	v_lshl_add_u32 v134, v124, 2, s3
	v_lshl_add_u64 v[66:67], v[36:37], 1, v[34:35]
	v_lshl_add_u64 v[68:69], v[68:69], 1, s[4:5]
	s_movk_i32 s2, 0x1a00
	v_lshlrev_b32_e32 v48, 1, v70
	v_add_u32_e32 v135, v71, v73
	s_mov_b32 s3, 0xbfb8aa3b
	s_mov_b32 s59, 0x800000
	s_mov_b32 s65, 0x3f317217
	s_mov_b32 s66, 0x7f800000
	s_mov_b32 s58, 0x3d800000
	s_mov_b32 s60, 0x3e000000
	v_add_u32_e32 v136, v76, v77
	v_add_u32_e32 v137, v79, v77
	v_add_u32_e32 v138, v80, v77
	v_add_u32_e32 v139, v33, v77
	v_mov_b32_e32 v140, 0x358637bd
	s_mov_b32 s67, 0xf800000
	v_mov_b32_e32 v141, 0x260
	v_mov_b32_e32 v142, 0x41b17218
	v_add_u32_e32 v143, v72, v75
	v_add_u32_e32 v144, v72, v78
	v_add_u32_e32 v145, v74, v32
	v_readlane_b32 s68, v242, 0
	s_waitcnt vmcnt(0)
	s_branch .LBB0_459

.LBB0_463:
	s_waitcnt vmcnt(16)
	v_cvt_f32_fp8_e32 v32, v52
	v_cvt_f32_fp8_sdwa v33, v52 src0_sel:BYTE_1
	v_cvt_f32_fp8_sdwa v34, v52 src0_sel:BYTE_2
	v_cvt_f32_fp8_sdwa v35, v52 src0_sel:BYTE_3
	v_cvt_f32_fp8_e32 v36, v53
	v_cvt_f32_fp8_sdwa v37, v53 src0_sel:BYTE_1
	v_cvt_f32_fp8_sdwa v38, v53 src0_sel:BYTE_2
	v_cvt_f32_fp8_sdwa v39, v53 src0_sel:BYTE_3
	v_cvt_pk_bf16_f32 v32, v32, v33
	v_cvt_pk_bf16_f32 v33, v34, v35
	v_cvt_pk_bf16_f32 v34, v36, v37
	v_cvt_pk_bf16_f32 v35, v38, v39
	v_add_u32_e32 v36, v122, v128
	ds_write_b64 v118, v[42:43]
	ds_write_b16 v120, v4
	ds_write_b16_d16_hi v120, v4 offset:144
	ds_write_b16 v120, v5 offset:288
	ds_write_b16_d16_hi v120, v5 offset:432
	ds_write_b16 v120, v6 offset:576
	ds_write_b16_d16_hi v120, v6 offset:720
	ds_write_b16 v120, v7 offset:864
	ds_write_b16_d16_hi v120, v7 offset:1008
	ds_write_b16 v121, v12
	ds_write_b16_d16_hi v121, v12 offset:144
	ds_write_b16 v121, v13 offset:288
	ds_write_b16_d16_hi v121, v13 offset:432
	ds_write_b16 v121, v14 offset:576
	ds_write_b16_d16_hi v121, v14 offset:720
	ds_write_b16 v121, v15 offset:864
	ds_write_b16_d16_hi v121, v15 offset:1008
	ds_write_b128 v36, v[32:35] offset:55296
	v_cvt_f32_fp8_e32 v32, v56
	v_cvt_f32_fp8_sdwa v33, v56 src0_sel:BYTE_1
	v_cvt_f32_fp8_sdwa v34, v56 src0_sel:BYTE_2
	v_cvt_f32_fp8_sdwa v35, v56 src0_sel:BYTE_3
	v_cvt_f32_fp8_e32 v36, v57
	v_cvt_f32_fp8_sdwa v37, v57 src0_sel:BYTE_1
	v_cvt_f32_fp8_sdwa v38, v57 src0_sel:BYTE_2
	v_cvt_f32_fp8_sdwa v39, v57 src0_sel:BYTE_3
	v_cvt_pk_bf16_f32 v32, v32, v33
	v_cvt_pk_bf16_f32 v33, v34, v35
	v_cvt_pk_bf16_f32 v34, v36, v37
	v_cvt_pk_bf16_f32 v35, v38, v39
	v_add_u32_e32 v36, v122, v129
	ds_write_b128 v36, v[32:35] offset:55296
	v_cvt_f32_fp8_e32 v32, v58
	v_cvt_f32_fp8_sdwa v33, v58 src0_sel:BYTE_1
	v_cvt_f32_fp8_sdwa v34, v58 src0_sel:BYTE_2
	v_cvt_f32_fp8_sdwa v35, v58 src0_sel:BYTE_3
	v_cvt_f32_fp8_e32 v36, v59
	v_cvt_f32_fp8_sdwa v37, v59 src0_sel:BYTE_1
	v_cvt_f32_fp8_sdwa v38, v59 src0_sel:BYTE_2
	v_cvt_f32_fp8_sdwa v39, v59 src0_sel:BYTE_3
	v_cvt_pk_bf16_f32 v32, v32, v33
	v_cvt_pk_bf16_f32 v33, v34, v35
	v_cvt_pk_bf16_f32 v34, v36, v37
	v_cvt_pk_bf16_f32 v35, v38, v39
	v_add_u32_e32 v36, v123, v128
	ds_write_b128 v36, v[32:35] offset:18432
	v_cvt_f32_fp8_e32 v32, v60
	v_cvt_f32_fp8_sdwa v33, v60 src0_sel:BYTE_1
	v_cvt_f32_fp8_sdwa v34, v60 src0_sel:BYTE_2
	v_cvt_f32_fp8_sdwa v35, v60 src0_sel:BYTE_3
	v_cvt_f32_fp8_e32 v36, v61
	v_cvt_f32_fp8_sdwa v37, v61 src0_sel:BYTE_1
	v_cvt_f32_fp8_sdwa v38, v61 src0_sel:BYTE_2
	v_cvt_f32_fp8_sdwa v39, v61 src0_sel:BYTE_3
	v_cvt_pk_bf16_f32 v32, v32, v33
	v_cvt_pk_bf16_f32 v33, v34, v35
	v_cvt_pk_bf16_f32 v34, v36, v37
	v_cvt_pk_bf16_f32 v35, v38, v39
	v_add_u32_e32 v36, v123, v129
	v_add_u32_e32 v86, s69, v124
	ds_write_b128 v36, v[32:35] offset:18432
	v_mad_i64_i32 v[32:33], s[0:1], v86, s2, v[66:67]
	v_add_u32_e32 v34, 1, v86
	s_waitcnt lgkmcnt(0)
	s_barrier
	v_mad_i64_i32 v[34:35], s[0:1], v34, s2, v[66:67]
	global_load_ushort v161, v[32:33], off offset:3584
	global_load_ushort v160, v[32:33], off offset:3616
	global_load_ushort v159, v[32:33], off offset:3648
	global_load_ushort v158, v[32:33], off offset:3680
	global_load_ushort v157, v[34:35], off offset:3584
	global_load_ushort v156, v[34:35], off offset:3616
	global_load_ushort v155, v[34:35], off offset:3648
	global_load_ushort v154, v[34:35], off offset:3680
	v_add_u32_e32 v32, 2, v86
	v_mad_i64_i32 v[32:33], s[0:1], v32, s2, v[66:67]
	v_add_u32_e32 v34, 3, v86
	v_mad_i64_i32 v[34:35], s[0:1], v34, s2, v[66:67]
	global_load_ushort v153, v[32:33], off offset:3584
	global_load_ushort v152, v[32:33], off offset:3616
	global_load_ushort v151, v[32:33], off offset:3648
	global_load_ushort v150, v[32:33], off offset:3680
	global_load_ushort v149, v[34:35], off offset:3584
	global_load_ushort v148, v[34:35], off offset:3616
	global_load_ushort v147, v[34:35], off offset:3648
	global_load_ushort v146, v[34:35], off offset:3680
	v_readlane_b32 s0, v242, 11
	s_add_i32 s68, s68, s0
	s_cmpk_gt_i32 s68, 0x87f
	s_cselect_b64 s[62:63], -1, 0
	s_and_b64 vcc, exec, s[62:63]
	v_mov_b64_e32 v[76:77], v[16:17]
	v_mov_b64_e32 v[78:79], v[22:23]
	v_mov_b64_e32 v[70:71], v[24:25]
	v_mov_b64_e32 v[72:73], v[30:31]
	v_mov_b64_e32 v[84:85], v[18:19]
	v_mov_b64_e32 v[80:81], v[20:21]
	v_mov_b64_e32 v[82:83], v[26:27]
	v_mov_b64_e32 v[74:75], v[28:29]
	v_readlane_b32 s1, v242, 12
	s_cbranch_vccnz .LBB0_469
	s_ashr_i32 s0, s68, 2
	s_mul_hi_i32 s1, s0, 0x78787879
	s_lshr_b32 s33, s1, 31
	s_ashr_i32 s48, s1, 5
	s_add_i32 s48, s48, s33
	s_mul_i32 s1, s48, 0x44
	s_sub_i32 s33, s0, s1
	s_lshl_b32 s70, s33, 6
	s_cmp_gt_i32 s33, 3
	s_mov_b64 s[0:1], -1
	s_cbranch_scc0 .LBB0_466
	s_lshl_b32 s0, s48, 12
	s_add_i32 s0, s70, s0
	s_add_i32 s49, s0, 0xffffff00
	s_mov_b64 s[0:1], 0

.LBB0_2287:
	s_add_u32 s8, s0, 0x11fff000
	s_addc_u32 s9, s1, 0
	v_and_b32_e32 v87, 63, v24
	s_waitcnt vmcnt(7)
	v_cvt_pk_bf16_f32 v4, v4, v8
	v_add_u32_e32 v8, s5, v87
	s_movk_i32 s4, 0x1a00
	v_mov_b64_e32 v[32:33], s[8:9]
	s_waitcnt vmcnt(5)
	v_cvt_pk_bf16_f32 v5, v5, v9
	v_mad_i64_i32 v[8:9], s[2:3], v8, s4, v[32:33]
	v_add_u32_e32 v35, s5, v86
	s_add_u32 s10, s0, 0x240ff000
	v_readlane_b32 s2, v242, 24
	v_add_u32_e32 v21, 48, v35
	s_addc_u32 s11, s1, 0
	s_lshl_b32 s12, s2, 1
	v_mad_i64_i32 v[36:37], s[2:3], v21, s4, v[32:33]
	s_mov_b32 s13, 0
	v_readlane_b32 s2, v242, 20
	s_lshl_b32 s2, s2, 1
	s_mov_b32 s3, s13
	v_lshl_add_u64 v[36:37], v[36:37], 0, s[2:3]
	v_lshlrev_b32_e32 v20, 1, v20
	v_mov_b32_e32 v21, 0
	v_and_b32_e32 v28, 12, v28
	v_add_u32_e32 v38, 32, v35
	v_lshl_add_u64 v[36:37], v[36:37], 0, v[20:21]
	v_lshlrev_b32_e32 v28, 1, v28
	v_mov_b32_e32 v29, v21
	v_mad_i64_i32 v[38:39], s[6:7], v38, s4, v[32:33]
	v_lshl_add_u64 v[36:37], v[36:37], 0, v[28:29]
	s_movk_i32 s14, 0x1000
	v_lshl_add_u64 v[38:39], v[38:39], 0, s[2:3]
	v_add_u32_e32 v40, 16, v35
	v_add_co_u32_e32 v36, vcc, s14, v36
	v_lshl_add_u64 v[38:39], v[38:39], 0, v[20:21]
	v_mad_i64_i32 v[40:41], s[6:7], v40, s4, v[32:33]
	v_addc_co_u32_e32 v37, vcc, 0, v37, vcc
	v_lshl_add_u64 v[38:39], v[38:39], 0, v[28:29]
	v_lshl_add_u64 v[40:41], v[40:41], 0, s[2:3]
	v_add_co_u32_e32 v38, vcc, s14, v38
	v_lshl_add_u64 v[40:41], v[40:41], 0, v[20:21]
	v_mad_i64_i32 v[42:43], s[6:7], v35, s4, v[32:33]
	v_add_u32_e32 v34, 0x200, v24
	v_addc_co_u32_e32 v39, vcc, 0, v39, vcc
	v_lshl_add_u64 v[40:41], v[40:41], 0, v[28:29]
	v_lshl_add_u64 v[42:43], v[42:43], 0, s[2:3]
	v_ashrrev_i32_e32 v31, 3, v34
	v_ashrrev_i32_e32 v88, 3, v24
	v_add_co_u32_e32 v40, vcc, s14, v40
	v_lshl_add_u64 v[42:43], v[42:43], 0, v[20:21]
	v_lshl_add_u64 v[8:9], v[8:9], 0, s[12:13]
	s_mov_b64 s[18:19], 0x1400
	v_and_b32_e32 v16, -8, v31
	v_and_b32_e32 v18, -8, v88
	v_addc_co_u32_e32 v41, vcc, 0, v41, vcc
	v_lshl_add_u64 v[42:43], v[42:43], 0, v[28:29]
	v_lshl_add_u64 v[8:9], v[8:9], 0, s[18:19]
	v_ashrrev_i32_e32 v17, 31, v16
	v_ashrrev_i32_e32 v19, 31, v18
	v_add_co_u32_e32 v48, vcc, s14, v42
	v_add_u32_e32 v35, s5, v88
	v_lshl_add_u64 v[10:11], v[16:17], 1, v[8:9]
	v_lshl_add_u64 v[8:9], v[18:19], 1, v[8:9]
	v_addc_co_u32_e32 v49, vcc, 0, v43, vcc
	v_mad_i64_i32 v[32:33], s[6:7], v35, s4, v[32:33]
	v_lshlrev_b32_e32 v35, 2, v24
	global_load_dwordx4 v[12:15], v[10:11], off
	s_nop 0
	global_load_dwordx4 v[8:11], v[8:9], off
	s_nop 0
	global_load_dwordx2 v[42:43], v[36:37], off offset:512
	global_load_dwordx2 v[44:45], v[38:39], off offset:512
	global_load_dwordx2 v[46:47], v[40:41], off offset:512
	s_nop 0
	global_load_dwordx2 v[48:49], v[48:49], off offset:512
	v_and_b32_e32 v36, 28, v35
	v_lshlrev_b32_e32 v38, 1, v36
	v_mov_b32_e32 v39, v21
	v_lshl_add_u64 v[32:33], v[32:33], 0, v[38:39]
	v_add_co_u32_e32 v32, vcc, s14, v32
	s_waitcnt vmcnt(9)
	v_cvt_pk_bf16_f32 v6, v6, v26
	v_addc_co_u32_e32 v33, vcc, 0, v33, vcc
	global_load_dwordx2 v[32:33], v[32:33], off offset:2048
	s_waitcnt vmcnt(8)
	v_cvt_pk_bf16_f32 v25, v25, v27
	s_movk_i32 s3, 0x50
	v_and_b32_e32 v4, v7, v4
	v_and_b32_e32 v5, v7, v5
	v_and_b32_e32 v6, v7, v6
	v_and_b32_e32 v7, v7, v25
	v_mul_lo_u32 v25, v88, s3
	s_movk_i32 s3, 0x90
	v_add3_u32 v89, 0, v25, v38
	v_mul_lo_u32 v25, v18, s3
	v_lshlrev_b32_e32 v26, 1, v87
	v_add3_u32 v90, 0, v25, v26
	v_mul_lo_u32 v25, v16, s3
	v_add3_u32 v91, 0, v25, v26
	v_and_b32_e32 v25, 48, v24
	v_add_u32_e32 v39, 0, v25
	s_movk_i32 s5, 0xff
	v_ashrrev_i32_e32 v25, 2, v24
	v_lshl_add_u32 v37, v86, 1, 0
	v_cmp_lt_u32_e64 s[14:15], s5, v24
	v_and_b32_e32 v26, -16, v25
	s_movk_i32 s5, 0x2400
	v_mad_i32_i24 v50, v22, s5, v37
	v_lshl_or_b32 v94, v22, 5, s64
	v_or_b32_e32 v22, v26, v86
	v_lshl_add_u32 v38, v23, 4, 0
	v_mad_u64_u32 v[22:23], s[6:7], v22, s3, v[38:39]
	v_or_b32_e32 v23, v30, v26
	v_lshlrev_b32_e32 v26, 4, v24
	s_add_u32 s2, s8, s2
	v_and_b32_e32 v92, 0xc0, v35
	v_and_b32_e32 v41, 48, v25
	v_and_b32_e32 v26, 0x70, v26
	v_mul_lo_u32 v52, v88, s3
	v_mul_lo_u32 v55, v23, s3
	v_mul_lo_u32 v56, v31, s3
	v_ashrrev_i32_e32 v35, 31, v34
	s_addc_u32 s3, s9, 0
	v_add_u32_e32 v51, 0, v26
	v_lshlrev_b64 v[26:27], 3, v[34:35]
	v_lshl_add_u64 v[34:35], s[2:3], 0, v[20:21]
	v_lshlrev_b32_e32 v20, 2, v41
	v_or_b32_e32 v25, v30, v41
	v_lshl_add_u64 v[28:29], v[34:35], 0, v[28:29]
	v_lshl_add_u64 v[34:35], s[0:1], 0, v[20:21]
	v_lshlrev_b32_e32 v20, 2, v30
	v_mul_u32_u24_e32 v40, 0x50, v86
	v_mul_u32_u24_e32 v53, 0x90, v25
	v_mul_u32_u24_e32 v54, 0x90, v86
	v_ashrrev_i32_e32 v25, 31, v24
	v_lshl_add_u64 v[30:31], v[34:35], 0, v[20:21]
	s_mov_b64 s[0:1], 0x32af000
	v_or_b32_e32 v93, 60, v92
	v_cmp_ne_u32_e64 s[16:17], 0, v86
	v_lshlrev_b64 v[24:25], 3, v[24:25]
	v_lshl_add_u64 v[30:31], v[30:31], 0, s[0:1]
	s_movk_i32 s5, 0x44
	v_lshlrev_b32_e32 v20, 1, v36
	v_add_u32_e32 v23, v39, v40
	s_mov_b32 s21, 0xbfb8aa3b
	s_mov_b32 s24, 0x800000
	s_mov_b32 s25, 0x3f317217
	s_mov_b32 s26, 0x7f800000
	s_mov_b32 s20, 0x3d800000
	v_add_u32_e32 v95, v50, v53
	v_add_u32_e32 v96, v38, v54
	v_add_u32_e32 v97, v37, v55
	v_add_u32_e32 v98, v51, v52
	s_mov_b32 s27, 0xc3e00000
	v_add_u32_e32 v99, v51, v56
	v_mov_b32_e32 v100, 0x41b17218
	v_mov_b32_e32 v101, 0x44
	v_mov_b32_e32 v102, 0x43e00000
	v_readlane_b32 s2, v242, 0
	s_waitcnt vmcnt(4)
	v_mov_b64_e32 v[40:41], v[42:43]
	s_waitcnt vmcnt(3)
	v_mov_b64_e32 v[38:39], v[44:45]
	s_waitcnt vmcnt(1)
	v_mov_b64_e32 v[34:35], v[48:49]
	v_mov_b64_e32 v[36:37], v[46:47]
	s_waitcnt vmcnt(0)
	s_branch .LBB0_2289

.LBB0_2289:
	v_readlane_b32 s0, v242, 11
	s_add_i32 s28, s2, s0
	s_cmpk_gt_i32 s28, 0x87f
	s_cselect_b64 s[22:23], -1, 0
	s_and_b64 vcc, exec, s[22:23]
	s_waitcnt vmcnt(4)
	ds_write_b64 v89, v[32:33] offset:36864
	ds_write_b16 v90, v8
	ds_write_b16_d16_hi v90, v8 offset:144
	ds_write_b16 v90, v9 offset:288
	ds_write_b16_d16_hi v90, v9 offset:432
	ds_write_b16 v90, v10 offset:576
	ds_write_b16_d16_hi v90, v10 offset:720
	ds_write_b16 v90, v11 offset:864
	ds_write_b16_d16_hi v90, v11 offset:1008
	ds_write_b16 v91, v12
	ds_write_b16_d16_hi v91, v12 offset:144
	ds_write_b16 v91, v13 offset:288
	ds_write_b16_d16_hi v91, v13 offset:432
	ds_write_b16 v91, v14 offset:576
	ds_write_b16_d16_hi v91, v14 offset:720
	ds_write_b16 v91, v15 offset:864
	ds_write_b16_d16_hi v91, v15 offset:1008
	s_waitcnt lgkmcnt(0)
	s_barrier
	v_readlane_b32 s1, v242, 12
	s_cbranch_vccnz .LBB0_2295
	s_ashr_i32 s0, s28, 2
	s_mul_hi_i32 s1, s0, 0x78787879
	s_lshr_b32 s3, s1, 31
	s_ashr_i32 s6, s1, 5
	s_add_i32 s6, s6, s3
	s_mul_i32 s1, s6, 0x44
	s_sub_i32 s0, s0, s1
	s_lshl_b32 s7, s0, 6
	s_cmp_gt_i32 s0, 3
	s_mov_b64 s[0:1], -1
	s_cbranch_scc0 .LBB0_2292
	s_lshl_b32 s0, s6, 12
	s_add_i32 s0, s7, s0
	s_add_i32 s3, s0, 0xffffff00
	s_mov_b64 s[0:1], 0

.LBB0_2423:
	s_add_u32 s8, s0, 0x1fcff000
	s_addc_u32 s9, s1, 0
	v_readlane_b32 s0, v242, 25
	v_readlane_b32 s1, v242, 26
	v_lshlrev_b32_e32 v33, 2, v8
	s_and_b64 vcc, exec, s[0:1]
	s_cbranch_vccnz .LBB0_2457
	s_waitcnt vmcnt(11)
	v_cvt_pk_bf16_f32 v8, v9, v39
	s_waitcnt vmcnt(5)
	v_cvt_pk_bf16_f32 v39, v46, v48
	v_lshlrev_b32_e32 v48, 2, v40
	v_ashrrev_i32_e32 v117, 3, v40
	s_movk_i32 s0, 0x50
	v_and_b32_e32 v70, 28, v48
	v_cvt_pk_bf16_f32 v9, v10, v44
	v_mul_lo_u32 v41, v117, s0
	s_add_i32 s0, 0, 0x1c200
	v_lshlrev_b32_e32 v44, 1, v70
	v_add_u32_e32 v54, 0x200, v40
	v_add3_u32 v118, s0, v41, v44
	v_and_b32_e32 v119, 63, v40
	v_and_b32_e32 v44, -8, v117
	s_movk_i32 s1, 0x90
	v_ashrrev_i32_e32 v62, 3, v54
	v_cvt_pk_bf16_f32 v10, v45, v47
	v_mul_lo_u32 v41, v44, s1
	v_lshlrev_b32_e32 v45, 1, v119
	v_and_b32_e32 v46, -8, v62
	v_add3_u32 v120, 0, v41, v45
	v_mul_lo_u32 v41, v46, s1
	v_and_b32_e32 v8, v11, v8
	v_and_b32_e32 v9, v11, v9
	v_and_b32_e32 v10, v11, v10
	v_and_b32_e32 v11, v11, v39
	v_bfe_u32 v39, v40, 6, 2
	v_add3_u32 v121, 0, v41, v45
	v_lshlrev_b32_e32 v41, 4, v40
	v_and_b32_e32 v64, 12, v38
	v_and_b32_e32 v38, 48, v40
	v_and_b32_e32 v41, 0x70, v41
	v_lshlrev_b32_e32 v63, 4, v39
	v_add_u32_e32 v71, s0, v38
	s_movk_i32 s0, 0xff
	v_mul_i32_i24_e32 v38, 0x1200, v37
	v_add_u32_e32 v122, 0, v41
	v_or_b32_e32 v124, v33, v63
	v_ashrrev_i32_e32 v41, 31, v40
	v_cmp_lt_u32_e64 s[14:15], s0, v40
	v_or3_b32 v33, v63, v38, v33
	s_movk_i32 s0, 0x48
	v_lshlrev_b64 v[50:51], 3, v[40:41]
	v_and_b32_e32 v41, 0xc0, v48
	v_lshlrev_b32_e32 v48, 1, v37
	v_or_b32_e32 v63, v63, v112
	v_add_u32_e32 v38, 0, v32
	v_mad_u32_u24 v33, v112, s0, v33
	v_mad_u32_u24 v126, v63, s1, v38
	v_mul_u32_u24_e32 v63, 0x48, v63
	v_and_b32_e32 v65, 0xffffff00, v40
	s_add_i32 s3, 0, 0x1c000
	v_lshlrev_b32_e32 v66, 6, v39
	v_readlane_b32 s6, v242, 24
	v_lshl_add_u32 v130, v33, 1, 0
	v_or_b32_e32 v33, 1, v48
	s_add_i32 s2, 0, 0x16800
	v_lshlrev_b32_e32 v63, 1, v63
	v_add3_u32 v73, s3, v65, v66
	v_or_b32_e32 v65, s6, v112
	v_mul_lo_u32 v129, v62, s1
	v_lshl_or_b32 v62, v33, 4, v112
	v_lshl_or_b32 v37, v37, 5, v112
	v_add3_u32 v127, s2, v63, v32
	v_or_b32_e32 v63, v34, v112
	v_add_u32_e32 v68, v65, v34
	v_cmp_le_i32_e64 s[22:23], v48, v39
	v_lshlrev_b32_e32 v65, 1, v37
	v_or_b32_e32 v131, 1, v124
	v_or_b32_e32 v132, 2, v124
	v_or_b32_e32 v133, 3, v124
	v_cmp_lt_i32_e64 s[34:35], v48, v39
	v_cmp_ge_i32_e64 s[36:37], v48, v39
	v_lshlrev_b32_e32 v48, 1, v62
	s_add_i32 s0, 0, 0x18c00
	v_mul_lo_u32 v128, v117, s1
	v_cmp_gt_i32_e64 s[18:19], v62, v124
	v_cmp_lt_i32_e64 s[20:21], v62, v124
	v_mul_lo_u32 v74, v37, s1
	v_mul_lo_u32 v77, v62, s1
	v_cmp_gt_i32_e64 s[38:39], v62, v131
	v_cmp_gt_i32_e64 s[40:41], v62, v132
	v_cmp_gt_i32_e64 s[42:43], v62, v133
	v_add_u32_e32 v79, s0, v65
	v_cmp_ge_i32_e64 s[50:51], v33, v39
	v_add_u32_e32 v33, s0, v48
	v_cmp_lt_i32_e64 s[52:53], v62, v132
	v_cmp_lt_i32_e64 s[54:55], v62, v133
	v_mad_u64_u32 v[62:63], s[0:1], v63, s1, v[38:39]
	v_readlane_b32 s0, v242, 20
	s_lshl_b32 s0, s0, 1
	s_add_u32 s0, s10, s0
	v_mov_b32_e32 v49, 0
	v_add_u32_e32 v78, s2, v48
	s_addc_u32 s1, s11, 0
	v_lshlrev_b32_e32 v48, 1, v36
	s_lshl_b32 s60, s6, 1
	v_cmp_gt_i32_e64 s[24:25], v37, v124
	v_cmp_gt_i32_e64 s[26:27], v37, v131
	v_cmp_gt_i32_e64 s[28:29], v37, v132
	v_cmp_gt_i32_e64 s[30:31], v37, v133
	v_cmp_lt_i32_e64 s[44:45], v37, v124
	v_cmp_lt_i32_e64 s[46:47], v37, v132
	v_cmp_lt_i32_e64 s[48:49], v37, v133
	v_lshl_add_u64 v[36:37], s[0:1], 0, v[48:49]
	v_lshlrev_b32_e32 v48, 1, v64
	s_add_u32 s0, s10, s60
	v_add_u32_e32 v75, s2, v65
	v_lshl_add_u64 v[64:65], v[36:37], 0, v[48:49]
	s_addc_u32 s1, s11, 0
	v_lshlrev_b32_e32 v48, 1, v112
	v_ashrrev_i32_e32 v55, 31, v54
	v_mul_u32_u24_e32 v72, 0x50, v112
	v_mul_u32_u24_e32 v76, 0x90, v124
	v_ashrrev_i32_e32 v69, 31, v68
	v_lshl_add_u64 v[36:37], s[0:1], 0, v[48:49]
	s_mov_b32 s61, 0
	v_add_u32_e32 v123, 0xd800, v122
	v_ashrrev_i32_e32 v45, 31, v44
	v_ashrrev_i32_e32 v47, 31, v46
	v_lshlrev_b64 v[54:55], 3, v[54:55]
	v_or_b32_e32 v125, 60, v41
	v_cmp_eq_u32_e64 s[16:17], 0, v112
	v_add_u32_e32 v63, 0xd800, v62
	v_lshl_add_u32 v134, v124, 2, s3
	v_lshl_add_u64 v[66:67], v[34:35], 1, v[36:37]
	v_lshl_add_u64 v[68:69], v[68:69], 1, s[8:9]
	s_movk_i32 s2, 0x1a00
	v_lshlrev_b32_e32 v48, 1, v70
	v_add_u32_e32 v135, v71, v72
	s_mov_b32 s3, 0xbfb8aa3b
	s_mov_b32 s12, 0x800000
	s_mov_b32 s13, 0x3f317217
	s_mov_b32 s63, 0x7f800000
	s_mov_b32 s62, 0x3d800000
	s_mov_b32 s64, 0x3e000000
	v_add_u32_e32 v136, v75, v76
	v_add_u32_e32 v137, v78, v76
	v_add_u32_e32 v138, v79, v76
	v_add_u32_e32 v139, v33, v76
	v_mov_b32_e32 v140, 0x358637bd
	s_mov_b32 s65, 0xf800000
	v_mov_b32_e32 v141, 0x260
	v_mov_b32_e32 v142, 0x41b17218
	v_add_u32_e32 v143, v38, v74
	v_add_u32_e32 v144, v38, v77
	v_add_u32_e32 v145, v73, v32
	v_readlane_b32 s68, v242, 0
	s_waitcnt vmcnt(0)
	s_branch .LBB0_2426

.LBB0_2430:
	s_waitcnt vmcnt(16)
	v_cvt_f32_fp8_e32 v32, v52
	v_cvt_f32_fp8_sdwa v33, v52 src0_sel:BYTE_1
	v_cvt_f32_fp8_sdwa v34, v52 src0_sel:BYTE_2
	v_cvt_f32_fp8_sdwa v35, v52 src0_sel:BYTE_3
	v_cvt_f32_fp8_e32 v36, v53
	v_cvt_f32_fp8_sdwa v37, v53 src0_sel:BYTE_1
	v_cvt_f32_fp8_sdwa v38, v53 src0_sel:BYTE_2
	v_cvt_f32_fp8_sdwa v39, v53 src0_sel:BYTE_3
	v_cvt_pk_bf16_f32 v32, v32, v33
	v_cvt_pk_bf16_f32 v33, v34, v35
	v_cvt_pk_bf16_f32 v34, v36, v37
	v_cvt_pk_bf16_f32 v35, v38, v39
	v_add_u32_e32 v36, v122, v128
	ds_write_b64 v118, v[42:43]
	ds_write_b16 v120, v4
	ds_write_b16_d16_hi v120, v4 offset:144
	ds_write_b16 v120, v5 offset:288
	ds_write_b16_d16_hi v120, v5 offset:432
	ds_write_b16 v120, v6 offset:576
	ds_write_b16_d16_hi v120, v6 offset:720
	ds_write_b16 v120, v7 offset:864
	ds_write_b16_d16_hi v120, v7 offset:1008
	ds_write_b16 v121, v12
	ds_write_b16_d16_hi v121, v12 offset:144
	ds_write_b16 v121, v13 offset:288
	ds_write_b16_d16_hi v121, v13 offset:432
	ds_write_b16 v121, v14 offset:576
	ds_write_b16_d16_hi v121, v14 offset:720
	ds_write_b16 v121, v15 offset:864
	ds_write_b16_d16_hi v121, v15 offset:1008
	ds_write_b128 v36, v[32:35] offset:55296
	v_cvt_f32_fp8_e32 v32, v56
	v_cvt_f32_fp8_sdwa v33, v56 src0_sel:BYTE_1
	v_cvt_f32_fp8_sdwa v34, v56 src0_sel:BYTE_2
	v_cvt_f32_fp8_sdwa v35, v56 src0_sel:BYTE_3
	v_cvt_f32_fp8_e32 v36, v57
	v_cvt_f32_fp8_sdwa v37, v57 src0_sel:BYTE_1
	v_cvt_f32_fp8_sdwa v38, v57 src0_sel:BYTE_2
	v_cvt_f32_fp8_sdwa v39, v57 src0_sel:BYTE_3
	v_cvt_pk_bf16_f32 v32, v32, v33
	v_cvt_pk_bf16_f32 v33, v34, v35
	v_cvt_pk_bf16_f32 v34, v36, v37
	v_cvt_pk_bf16_f32 v35, v38, v39
	v_add_u32_e32 v36, v122, v129
	ds_write_b128 v36, v[32:35] offset:55296
	v_cvt_f32_fp8_e32 v32, v58
	v_cvt_f32_fp8_sdwa v33, v58 src0_sel:BYTE_1
	v_cvt_f32_fp8_sdwa v34, v58 src0_sel:BYTE_2
	v_cvt_f32_fp8_sdwa v35, v58 src0_sel:BYTE_3
	v_cvt_f32_fp8_e32 v36, v59
	v_cvt_f32_fp8_sdwa v37, v59 src0_sel:BYTE_1
	v_cvt_f32_fp8_sdwa v38, v59 src0_sel:BYTE_2
	v_cvt_f32_fp8_sdwa v39, v59 src0_sel:BYTE_3
	v_cvt_pk_bf16_f32 v32, v32, v33
	v_cvt_pk_bf16_f32 v33, v34, v35
	v_cvt_pk_bf16_f32 v34, v36, v37
	v_cvt_pk_bf16_f32 v35, v38, v39
	v_add_u32_e32 v36, v123, v128
	ds_write_b128 v36, v[32:35] offset:18432
	v_cvt_f32_fp8_e32 v32, v60
	v_cvt_f32_fp8_sdwa v33, v60 src0_sel:BYTE_1
	v_cvt_f32_fp8_sdwa v34, v60 src0_sel:BYTE_2
	v_cvt_f32_fp8_sdwa v35, v60 src0_sel:BYTE_3
	v_cvt_f32_fp8_e32 v36, v61
	v_cvt_f32_fp8_sdwa v37, v61 src0_sel:BYTE_1
	v_cvt_f32_fp8_sdwa v38, v61 src0_sel:BYTE_2
	v_cvt_f32_fp8_sdwa v39, v61 src0_sel:BYTE_3
	v_cvt_pk_bf16_f32 v32, v32, v33
	v_cvt_pk_bf16_f32 v33, v34, v35
	v_cvt_pk_bf16_f32 v34, v36, v37
	v_cvt_pk_bf16_f32 v35, v38, v39
	v_add_u32_e32 v36, v123, v129
	v_add_u32_e32 v86, s69, v124
	ds_write_b128 v36, v[32:35] offset:18432
	v_mad_i64_i32 v[32:33], s[0:1], v86, s2, v[66:67]
	v_add_u32_e32 v34, 1, v86
	s_waitcnt lgkmcnt(0)
	s_barrier
	v_mad_i64_i32 v[34:35], s[0:1], v34, s2, v[66:67]
	global_load_ushort v161, v[32:33], off offset:3584
	global_load_ushort v160, v[32:33], off offset:3616
	global_load_ushort v159, v[32:33], off offset:3648
	global_load_ushort v158, v[32:33], off offset:3680
	global_load_ushort v157, v[34:35], off offset:3584
	global_load_ushort v156, v[34:35], off offset:3616
	global_load_ushort v155, v[34:35], off offset:3648
	global_load_ushort v154, v[34:35], off offset:3680
	v_add_u32_e32 v32, 2, v86
	v_mad_i64_i32 v[32:33], s[0:1], v32, s2, v[66:67]
	v_add_u32_e32 v34, 3, v86
	v_mad_i64_i32 v[34:35], s[0:1], v34, s2, v[66:67]
	global_load_ushort v153, v[32:33], off offset:3584
	global_load_ushort v152, v[32:33], off offset:3616
	global_load_ushort v151, v[32:33], off offset:3648
	global_load_ushort v150, v[32:33], off offset:3680
	global_load_ushort v149, v[34:35], off offset:3584
	global_load_ushort v148, v[34:35], off offset:3616
	global_load_ushort v147, v[34:35], off offset:3648
	global_load_ushort v146, v[34:35], off offset:3680
	v_readlane_b32 s0, v242, 11
	s_add_i32 s68, s68, s0
	s_cmpk_gt_i32 s68, 0x87f
	s_cselect_b64 s[66:67], -1, 0
	s_and_b64 vcc, exec, s[66:67]
	v_mov_b64_e32 v[76:77], v[16:17]
	v_mov_b64_e32 v[78:79], v[22:23]
	v_mov_b64_e32 v[70:71], v[24:25]
	v_mov_b64_e32 v[72:73], v[30:31]
	v_mov_b64_e32 v[84:85], v[18:19]
	v_mov_b64_e32 v[80:81], v[20:21]
	v_mov_b64_e32 v[82:83], v[26:27]
	v_mov_b64_e32 v[74:75], v[28:29]
	v_readlane_b32 s1, v242, 12
	s_cbranch_vccnz .LBB0_2436
	s_ashr_i32 s0, s68, 2
	s_mul_hi_i32 s1, s0, 0x78787879
	s_lshr_b32 s6, s1, 31
	s_ashr_i32 s7, s1, 5
	s_add_i32 s7, s7, s6
	s_mul_i32 s1, s7, 0x44
	s_sub_i32 s6, s0, s1
	s_lshl_b32 s70, s6, 6
	s_cmp_gt_i32 s6, 3
	s_mov_b64 s[0:1], -1
	s_cbranch_scc0 .LBB0_2433
	s_lshl_b32 s0, s7, 12
	s_add_i32 s0, s70, s0
	s_add_i32 s33, s0, 0xffffff00
	s_mov_b64 s[0:1], 0
